# grid barrier poll loops: s_sleep 4 instead of s_sleep 1 between polls of the arrival counter (fewer polls hammering the one counter word while workgroups wait)
# baseline (speedup 1.0000x reference)
.LBB0_55:
	global_load_dword v16, v17, s[8:9] sc1
	global_load_dword v1, v17, s[10:11] sc1
	global_load_dword v2, v17, s[20:21] sc1
	global_load_dword v3, v17, s[22:23] sc1
	global_load_dword v4, v17, s[24:25] sc1
	global_load_dword v5, v17, s[26:27] sc1
	global_load_dword v6, v17, s[28:29] sc1
	global_load_dword v7, v17, s[30:31] sc1
	global_load_dword v8, v17, s[34:35] sc1
	global_load_dword v9, v17, s[38:39] sc1
	global_load_dword v10, v17, s[46:47] sc1
	global_load_dword v11, v17, s[48:49] sc1
	global_load_dword v12, v17, s[50:51] sc1
	global_load_dword v13, v17, s[52:53] sc1
	global_load_dword v14, v17, s[54:55] sc1
	global_load_dword v15, v17, s[56:57] sc1
	s_mov_b64 s[58:59], -1
	s_mov_b64 s[60:61], -1
	s_waitcnt vmcnt(14)
	v_add_u32_e32 v18, v1, v16
	s_waitcnt vmcnt(13)
	v_add_u32_e32 v18, v18, v2
	s_waitcnt vmcnt(12)
	v_add_u32_e32 v18, v18, v3
	s_waitcnt vmcnt(11)
	v_add_u32_e32 v18, v18, v4
	s_waitcnt vmcnt(10)
	v_add_u32_e32 v18, v18, v5
	s_waitcnt vmcnt(9)
	v_add_u32_e32 v18, v18, v6
	s_waitcnt vmcnt(8)
	v_add_u32_e32 v18, v18, v7
	s_waitcnt vmcnt(7)
	v_add_u32_e32 v18, v18, v8
	s_waitcnt vmcnt(6)
	v_add_u32_e32 v18, v18, v9
	s_waitcnt vmcnt(5)
	v_add_u32_e32 v18, v18, v10
	s_waitcnt vmcnt(4)
	v_add_u32_e32 v18, v18, v11
	s_waitcnt vmcnt(3)
	v_add_u32_e32 v18, v18, v12
	s_waitcnt vmcnt(2)
	v_add_u32_e32 v18, v18, v13
	s_waitcnt vmcnt(1)
	v_add_u32_e32 v18, v18, v14
	s_waitcnt vmcnt(0)
	v_add_u32_e32 v18, v18, v15
	v_cmp_eq_u32_e32 vcc, s65, v18
	s_cbranch_vccnz .LBB0_54
	s_and_b32 s58, s66, 0xff
	s_cmp_eq_u32 s58, 0
	s_mov_b64 s[58:59], -1
	s_mov_b64 s[62:63], -1
	s_sleep 4
	s_cbranch_scc1 .LBB0_59
	s_and_b64 vcc, exec, s[62:63]
	s_cbranch_vccz .LBB0_54

.LBB0_73:
	s_and_b32 s30, s38, 0xff
	s_mov_b64 s[28:29], -1
	s_cmp_lg_u32 s30, 0
	s_mov_b64 s[34:35], -1
	s_sleep 4
	s_cbranch_scc0 .LBB0_76
	s_and_b64 vcc, exec, s[34:35]
	s_cbranch_vccz .LBB0_72

.LBB0_90:
	s_and_b32 s28, s38, 0xff
	s_cmp_lg_u32 s28, 0
	s_mov_b64 s[30:31], -1
	s_sleep 4
	s_cbranch_scc0 .LBB0_93
	s_mov_b64 s[34:35], -1
	s_and_b64 vcc, exec, s[30:31]
	s_cbranch_vccz .LBB0_89

.LBB0_253:
	global_load_dword v16, v17, s[8:9] sc1
	global_load_dword v1, v17, s[10:11] sc1
	global_load_dword v2, v17, s[12:13] sc1
	global_load_dword v3, v17, s[14:15] sc1
	global_load_dword v4, v17, s[16:17] sc1
	global_load_dword v5, v17, s[18:19] sc1
	global_load_dword v6, v17, s[20:21] sc1
	global_load_dword v7, v17, s[22:23] sc1
	global_load_dword v8, v17, s[24:25] sc1
	global_load_dword v9, v17, s[26:27] sc1
	global_load_dword v10, v17, s[28:29] sc1
	global_load_dword v11, v17, s[30:31] sc1
	global_load_dword v12, v17, s[34:35] sc1
	global_load_dword v13, v17, s[38:39] sc1
	global_load_dword v14, v17, s[46:47] sc1
	global_load_dword v15, v17, s[48:49] sc1
	s_mov_b64 s[50:51], -1
	s_mov_b64 s[52:53], -1
	s_waitcnt vmcnt(14)
	v_add_u32_e32 v18, v1, v16
	s_waitcnt vmcnt(13)
	v_add_u32_e32 v18, v18, v2
	s_waitcnt vmcnt(12)
	v_add_u32_e32 v18, v18, v3
	s_waitcnt vmcnt(11)
	v_add_u32_e32 v18, v18, v4
	s_waitcnt vmcnt(10)
	v_add_u32_e32 v18, v18, v5
	s_waitcnt vmcnt(9)
	v_add_u32_e32 v18, v18, v6
	s_waitcnt vmcnt(8)
	v_add_u32_e32 v18, v18, v7
	s_waitcnt vmcnt(7)
	v_add_u32_e32 v18, v18, v8
	s_waitcnt vmcnt(6)
	v_add_u32_e32 v18, v18, v9
	s_waitcnt vmcnt(5)
	v_add_u32_e32 v18, v18, v10
	s_waitcnt vmcnt(4)
	v_add_u32_e32 v18, v18, v11
	s_waitcnt vmcnt(3)
	v_add_u32_e32 v18, v18, v12
	s_waitcnt vmcnt(2)
	v_add_u32_e32 v18, v18, v13
	s_waitcnt vmcnt(1)
	v_add_u32_e32 v18, v18, v14
	s_waitcnt vmcnt(0)
	v_add_u32_e32 v18, v18, v15
	v_cmp_eq_u32_e32 vcc, s33, v18
	s_cbranch_vccnz .LBB0_252
	s_and_b32 s50, s56, 0xff
	s_cmp_eq_u32 s50, 0
	s_mov_b64 s[50:51], -1
	s_mov_b64 s[54:55], -1
	s_sleep 4
	s_cbranch_scc1 .LBB0_257
	s_and_b64 vcc, exec, s[54:55]
	s_cbranch_vccz .LBB0_252

.LBB0_271:
	s_and_b32 s22, s26, 0xff
	s_mov_b64 s[20:21], -1
	s_cmp_lg_u32 s22, 0
	s_mov_b64 s[24:25], -1
	s_sleep 4
	s_cbranch_scc0 .LBB0_274
	s_and_b64 vcc, exec, s[24:25]
	s_cbranch_vccz .LBB0_270

.LBB0_288:
	s_and_b32 s20, s26, 0xff
	s_cmp_lg_u32 s20, 0
	s_mov_b64 s[22:23], -1
	s_sleep 4
	s_cbranch_scc0 .LBB0_291
	s_mov_b64 s[24:25], -1
	s_and_b64 vcc, exec, s[22:23]
	s_cbranch_vccz .LBB0_287

.LBB0_3492:
	global_load_dword v16, v17, s[8:9] sc1
	global_load_dword v1, v17, s[10:11] sc1
	global_load_dword v2, v17, s[12:13] sc1
	global_load_dword v3, v17, s[14:15] sc1
	global_load_dword v4, v17, s[16:17] sc1
	global_load_dword v5, v17, s[18:19] sc1
	global_load_dword v6, v17, s[20:21] sc1
	global_load_dword v7, v17, s[22:23] sc1
	global_load_dword v8, v17, s[24:25] sc1
	global_load_dword v9, v17, s[26:27] sc1
	global_load_dword v10, v17, s[28:29] sc1
	global_load_dword v11, v17, s[30:31] sc1
	global_load_dword v12, v17, s[34:35] sc1
	global_load_dword v13, v17, s[36:37] sc1
	global_load_dword v14, v17, s[38:39] sc1
	global_load_dword v15, v17, s[46:47] sc1
	s_mov_b64 s[48:49], -1
	s_mov_b64 s[50:51], -1
	s_waitcnt vmcnt(14)
	v_add_u32_e32 v18, v1, v16
	s_waitcnt vmcnt(13)
	v_add_u32_e32 v18, v18, v2
	s_waitcnt vmcnt(12)
	v_add_u32_e32 v18, v18, v3
	s_waitcnt vmcnt(11)
	v_add_u32_e32 v18, v18, v4
	s_waitcnt vmcnt(10)
	v_add_u32_e32 v18, v18, v5
	s_waitcnt vmcnt(9)
	v_add_u32_e32 v18, v18, v6
	s_waitcnt vmcnt(8)
	v_add_u32_e32 v18, v18, v7
	s_waitcnt vmcnt(7)
	v_add_u32_e32 v18, v18, v8
	s_waitcnt vmcnt(6)
	v_add_u32_e32 v18, v18, v9
	s_waitcnt vmcnt(5)
	v_add_u32_e32 v18, v18, v10
	s_waitcnt vmcnt(4)
	v_add_u32_e32 v18, v18, v11
	s_waitcnt vmcnt(3)
	v_add_u32_e32 v18, v18, v12
	s_waitcnt vmcnt(2)
	v_add_u32_e32 v18, v18, v13
	s_waitcnt vmcnt(1)
	v_add_u32_e32 v18, v18, v14
	s_waitcnt vmcnt(0)
	v_add_u32_e32 v18, v18, v15
	v_cmp_eq_u32_e32 vcc, s33, v18
	s_cbranch_vccnz .LBB0_3491
	s_and_b32 s48, s54, 0xff
	s_cmp_eq_u32 s48, 0
	s_mov_b64 s[48:49], -1
	s_mov_b64 s[52:53], -1
	s_sleep 4
	s_cbranch_scc1 .LBB0_3496
	s_and_b64 vcc, exec, s[52:53]
	s_cbranch_vccz .LBB0_3491

.LBB0_3510:
	s_and_b32 s22, s3, 0xff
	s_mov_b64 s[20:21], -1
	s_cmp_lg_u32 s22, 0
	s_mov_b64 s[24:25], -1
	s_sleep 4
	s_cbranch_scc0 .LBB0_3513
	s_and_b64 vcc, exec, s[24:25]
	s_cbranch_vccz .LBB0_3509

.LBB0_3527:
	s_and_b32 s20, s3, 0xff
	s_cmp_lg_u32 s20, 0
	s_mov_b64 s[22:23], -1
	s_sleep 4
	s_cbranch_scc0 .LBB0_3530
	s_mov_b64 s[24:25], -1
	s_and_b64 vcc, exec, s[22:23]
	s_cbranch_vccz .LBB0_3526
